# v19: v10 + qknorm row loop waits for the prefetched next row at its first use (vmcnt(10) before the copy) instead of vmcnt(0) right after issuing it
# speedup vs baseline: 1.0086x; 1.0068x over previous
.LBB0_491:
	s_cmp_lt_i32 s72, 4
	s_cselect_b64 s[12:13], -1, 0
	s_and_b64 s[4:5], s[12:13], s[4:5]
	s_andn2_b64 vcc, exec, s[4:5]
	s_cbranch_vccnz .LBB0_508
	s_lshl_b32 s0, s2, 3
	s_add_i32 s24, s82, s0
	s_cmp_gt_i32 s24, 0x81ff
	s_cbranch_scc1 .LBB0_508
	s_load_dwordx2 s[4:5], s[74:75], 0x58
	s_load_dwordx2 s[6:7], s[74:75], 0x70
	s_lshl_b32 s3, s33, 3
	s_mul_i32 s1, s24, 0x2400
	v_and_b32_e32 v17, 63, v0
	s_mul_hi_i32 s0, s24, 0x2400
	s_waitcnt lgkmcnt(0)
	s_add_u32 s14, s54, s1
	v_mov_b32_e32 v3, 0
	v_lshlrev_b32_e32 v1, 3, v17
	v_lshlrev_b32_e32 v2, 2, v17
	s_addc_u32 s15, s55, s0
	global_load_dwordx2 v[4:5], v1, s[6:7]
	global_load_dwordx2 v[6:7], v1, s[4:5]
	v_lshl_add_u64 v[8:9], s[14:15], 0, v[2:3]
	s_mov_b64 s[4:5], 0x10e00000
	s_mov_b32 s19, 0x10e01000
	v_lshl_add_u64 v[18:19], v[8:9], 0, s[4:5]
	v_add_co_u32_e32 v20, vcc, s19, v8
	v_lshlrev_b32_e32 v1, 1, v0
	s_nop 0
	v_addc_co_u32_e32 v21, vcc, 0, v9, vcc
	global_load_dword v30, v[18:19], off offset:2048
	global_load_dword v16, v[18:19], off offset:2304
	global_load_dword v15, v[20:21], off offset:1024
	global_load_dword v14, v[20:21], off offset:1280
	global_load_dword v13, v[20:21], off offset:1536
	global_load_dword v12, v[20:21], off offset:1792
	global_load_dword v11, v[20:21], off offset:2048
	global_load_dword v10, v[20:21], off offset:2304
	global_load_dword v8, v[20:21], off offset:2560
	global_load_dword v9, v[20:21], off offset:2816
	v_and_b32_e32 v1, 30, v1
	v_cvt_f32_ubyte0_e32 v18, v1
	v_or_b32_e32 v1, 1, v1
	v_mul_f32_e32 v19, 0xbed49a78, v18
	s_mov_b32 s0, 0xc2fc0000
	v_cvt_f32_ubyte0_e32 v1, v1
	v_mov_b32_e32 v20, 0x42800000
	v_cmp_gt_f32_e32 vcc, s0, v19
	v_mul_f32_e32 v21, 0xbed49a78, v1
	v_cmp_gt_f32_e64 s[4:5], s0, v21
	v_cndmask_b32_e32 v19, 0, v20, vcc
	v_fmac_f32_e32 v19, 0xbed49a78, v18
	v_cndmask_b32_e64 v20, 0, v20, s[4:5]
	v_exp_f32_e32 v18, v19
	v_fmac_f32_e32 v20, 0xbed49a78, v1
	v_exp_f32_e32 v20, v20
	v_not_b32_e32 v19, 63
	s_add_i32 s0, s24, s3
	v_cndmask_b32_e32 v1, 0, v19, vcc
	s_mul_hi_i32 s1, s0, 0x2400
	s_mulk_i32 s0, 0x2400
	v_ldexp_f32 v1, v18, v1
	v_cndmask_b32_e64 v18, 0, v19, s[4:5]
	v_cmp_lt_u32_e64 s[4:5], 31, v17
	v_and_b32_e32 v17, 16, v0
	s_add_u32 s16, s54, s0
	v_ldexp_f32 v34, v20, v18
	v_cmp_eq_u32_e64 s[6:7], 0, v17
	s_mul_i32 s21, s33, 0x12000
	s_mul_hi_i32 s42, s3, 0x2400
	s_addc_u32 s17, s55, s1
	s_mov_b32 s43, 0x10e00000
	v_mov_b32_e32 v35, 0x358637bd
	s_brev_b32 s18, 60
	s_mov_b32 s44, 0x800000
	s_mov_b32 s20, 0x358637bd
	v_mbcnt_lo_u32_b32 v36, -1, 0
	v_mov_b32_e32 v37, v3
	v_mov_b32_e32 v38, v3
	v_mov_b32_e32 v39, v3
	v_mov_b32_e32 v40, v3
	v_mov_b32_e32 v41, v3
	v_mov_b32_e32 v42, v3
	v_mov_b32_e32 v43, v3
	v_mov_b32_e32 v44, v3
	v_mov_b32_e32 v45, v3
	v_mov_b32_e32 v46, v3
	s_waitcnt vmcnt(0)
	s_branch .LBB0_495
.LBB0_494:
	v_mov_b32_e32 v24, s61
	v_mov_b32_e32 v25, s50
	v_mov_b32_e32 v26, s58
	v_mov_b32_e32 v27, s46
	v_pk_add_f32 v[24:25], s[24:25], v[24:25]
	v_pk_add_f32 v[26:27], s[26:27], v[26:27]
	v_mov_b64_e32 v[54:55], s[20:21]
	v_pk_add_f32 v[24:25], v[24:25], v[26:27]
	v_cvt_pk_bf16_f32 v28, v28, v29
	v_pk_fma_f32 v[24:25], v[24:25], s[18:19], v[54:55] op_sel_hi:[1,0,0]
	global_store_dword v[32:33], v28, off offset:2304
	v_mul_f32_e32 v47, 0x4b800000, v25
	v_cmp_gt_f32_e32 vcc, s44, v25
	v_mov_b32_e32 v26, s62
	v_mov_b32_e32 v27, s51
	v_cndmask_b32_e32 v25, v25, v47, vcc
	v_rsq_f32_e32 v25, v25
	v_mov_b32_e32 v48, s59
	v_mov_b32_e32 v49, s47
	v_pk_add_f32 v[26:27], s[28:29], v[26:27]
	v_mul_f32_e32 v28, 0x45800000, v25
	v_cndmask_b32_e32 v28, v25, v28, vcc
	v_pk_mul_f32 v[22:23], v[28:29], v[22:23] op_sel_hi:[0,1]
	v_pk_mul_f32 v[22:23], v[4:5], v[22:23]
	v_cmp_gt_f32_e32 vcc, s44, v24
	v_cvt_pk_bf16_f32 v25, v22, v23
	v_mul_f32_e32 v22, 0x4b800000, v24
	v_cndmask_b32_e32 v22, v24, v22, vcc
	v_rsq_f32_e32 v24, v22
	v_add_co_u32_e64 v22, s[8:9], s19, v30
	v_pk_add_f32 v[48:49], s[30:31], v[48:49]
	s_nop 0
	v_addc_co_u32_e64 v23, s[8:9], 0, v31, s[8:9]
	global_store_dword v[22:23], v25, off offset:1024
	v_mul_f32_e32 v25, 0x45800000, v24
	v_pk_add_f32 v[26:27], v[26:27], v[48:49]
	v_cndmask_b32_e32 v24, v24, v25, vcc
	v_pk_mul_f32 v[20:21], v[24:25], v[20:21] op_sel_hi:[0,1]
	v_pk_fma_f32 v[24:25], v[26:27], s[18:19], v[54:55] op_sel_hi:[1,0,0]
	v_pk_mul_f32 v[20:21], v[4:5], v[20:21]
	v_mul_f32_e32 v26, 0x4b800000, v25
	v_cmp_gt_f32_e32 vcc, s44, v25
	v_cvt_pk_bf16_f32 v20, v20, v21
	global_store_dword v[22:23], v20, off offset:1280
	v_cndmask_b32_e32 v25, v25, v26, vcc
	v_rsq_f32_e32 v25, v25
	v_mov_b32_e32 v48, s63
	v_mov_b32_e32 v49, s56
	v_mov_b32_e32 v50, s60
	v_mul_f32_e32 v20, 0x45800000, v25
	v_cndmask_b32_e32 v20, v25, v20, vcc
	v_pk_mul_f32 v[18:19], v[20:21], v[18:19] op_sel_hi:[0,1]
	v_mul_f32_e32 v20, 0x4b800000, v24
	v_cmp_gt_f32_e32 vcc, s44, v24
	v_pk_mul_f32 v[18:19], v[4:5], v[18:19]
	v_mov_b32_e32 v51, s48
	v_cndmask_b32_e32 v20, v24, v20, vcc
	v_rsq_f32_e32 v20, v20
	v_cvt_pk_bf16_f32 v18, v18, v19
	v_pk_add_f32 v[48:49], s[34:35], v[48:49]
	v_pk_add_f32 v[50:51], s[36:37], v[50:51]
	global_store_dword v[22:23], v18, off offset:1536
	v_mul_f32_e32 v18, 0x45800000, v20
	v_pk_add_f32 v[48:49], v[48:49], v[50:51]
	v_cndmask_b32_e32 v18, v20, v18, vcc
	v_pk_mul_f32 v[16:17], v[18:19], v[16:17] op_sel_hi:[0,1]
	v_pk_fma_f32 v[18:19], v[48:49], s[18:19], v[54:55] op_sel_hi:[1,0,0]
	v_pk_mul_f32 v[16:17], v[4:5], v[16:17]
	v_mul_f32_e32 v20, 0x4b800000, v19
	v_cmp_gt_f32_e32 vcc, s44, v19
	v_cvt_pk_bf16_f32 v16, v16, v17
	global_store_dword v[22:23], v16, off offset:1792
	v_cndmask_b32_e32 v19, v19, v20, vcc
	v_rsq_f32_e32 v19, v19
	v_mov_b32_e32 v50, s65
	v_mov_b32_e32 v51, s57
	v_mov_b32_e32 v52, s64
	v_mul_f32_e32 v16, 0x45800000, v19
	v_cndmask_b32_e32 v16, v19, v16, vcc
	v_pk_mul_f32 v[14:15], v[16:17], v[14:15] op_sel_hi:[0,1]
	v_mul_f32_e32 v16, 0x4b800000, v18
	v_cmp_gt_f32_e32 vcc, s44, v18
	v_pk_mul_f32 v[14:15], v[4:5], v[14:15]
	v_mov_b32_e32 v53, s49
	v_cndmask_b32_e32 v16, v18, v16, vcc
	v_rsq_f32_e32 v16, v16
	v_cvt_pk_bf16_f32 v14, v14, v15
	v_pk_add_f32 v[50:51], s[38:39], v[50:51]
	v_pk_add_f32 v[52:53], s[40:41], v[52:53]
	global_store_dword v[22:23], v14, off offset:2048
	v_mul_f32_e32 v14, 0x45800000, v16
	v_pk_add_f32 v[50:51], v[50:51], v[52:53]
	v_cndmask_b32_e32 v14, v16, v14, vcc
	v_pk_mul_f32 v[12:13], v[14:15], v[12:13] op_sel_hi:[0,1]
	v_pk_fma_f32 v[14:15], v[50:51], s[18:19], v[54:55] op_sel_hi:[1,0,0]
	v_pk_mul_f32 v[12:13], v[4:5], v[12:13]
	v_mul_f32_e32 v16, 0x4b800000, v15
	v_cmp_gt_f32_e32 vcc, s44, v15
	v_cvt_pk_bf16_f32 v12, v12, v13
	global_store_dword v[22:23], v12, off offset:2304
	v_cndmask_b32_e32 v15, v15, v16, vcc
	v_rsq_f32_e32 v15, v15
	s_add_u32 s14, s14, s21
	s_addc_u32 s15, s15, s42
	s_add_u32 s16, s16, s21
	v_mul_f32_e32 v12, 0x45800000, v15
	v_cndmask_b32_e32 v12, v15, v12, vcc
	v_pk_mul_f32 v[10:11], v[12:13], v[10:11] op_sel_hi:[0,1]
	v_mul_f32_e32 v12, 0x4b800000, v14
	v_cmp_gt_f32_e32 vcc, s44, v14
	v_pk_mul_f32 v[10:11], v[4:5], v[10:11]
	s_addc_u32 s17, s17, s42
	v_cndmask_b32_e32 v12, v14, v12, vcc
	v_rsq_f32_e32 v12, v12
	v_cvt_pk_bf16_f32 v10, v10, v11
	global_store_dword v[22:23], v10, off offset:2560
	s_mov_b32 s24, s45
	v_mul_f32_e32 v10, 0x45800000, v12
	v_cndmask_b32_e32 v10, v12, v10, vcc
	v_pk_mul_f32 v[8:9], v[10:11], v[8:9] op_sel_hi:[0,1]
	v_pk_mul_f32 v[8:9], v[4:5], v[8:9]
	s_andn2_b64 vcc, exec, s[22:23]
	v_cvt_pk_bf16_f32 v8, v8, v9
	global_store_dword v[22:23], v8, off offset:2816
	s_waitcnt vmcnt(10)
	v_mov_b32_e32 v30, v37
	v_mov_b32_e32 v16, v38
	v_mov_b32_e32 v15, v39
	v_mov_b32_e32 v14, v40
	v_mov_b32_e32 v13, v41
	v_mov_b32_e32 v12, v42
	v_mov_b32_e32 v11, v43
	v_mov_b32_e32 v10, v44
	v_mov_b32_e32 v8, v45
	v_mov_b32_e32 v9, v46
	s_cbranch_vccz .LBB0_508

.LBB0_504:
	v_lshlrev_b32_e32 v28, 16, v16
	v_and_b32_e32 v29, 0xffff0000, v16
	v_pk_mul_f32 v[16:17], v[28:29], v[28:29]
	v_lshlrev_b32_e32 v22, 16, v15
	v_add_f32_e32 v31, v16, v17
	v_and_b32_e32 v23, 0xffff0000, v15
	v_pk_mul_f32 v[16:17], v[22:23], v[22:23]
	v_add_f32_dpp v31, v31, v31 quad_perm:[1,0,3,2] row_mask:0xf bank_mask:0xf bound_ctrl:1
	v_add_f32_e32 v47, v16, v17
	v_lshlrev_b32_e32 v20, 16, v14
	v_add_f32_dpp v31, v31, v31 quad_perm:[2,3,0,1] row_mask:0xf bank_mask:0xf bound_ctrl:1
	v_and_b32_e32 v21, 0xffff0000, v14
	v_pk_mul_f32 v[14:15], v[20:21], v[20:21]
	v_add_f32_dpp v31, v31, v31 row_half_mirror row_mask:0xf bank_mask:0xf bound_ctrl:1
	v_add_f32_e32 v48, v14, v15
	v_lshlrev_b32_e32 v18, 16, v13
	v_add_f32_dpp v31, v31, v31 row_mirror row_mask:0xf bank_mask:0xf bound_ctrl:1
	v_and_b32_e32 v19, 0xffff0000, v13
	v_readlane_b32 s66, v31, 0
	v_readlane_b32 s68, v31, 16
	v_readlane_b32 s67, v31, 32
	v_readlane_b32 s69, v31, 48
	v_add_f32_dpp v31, v47, v47 quad_perm:[1,0,3,2] row_mask:0xf bank_mask:0xf bound_ctrl:1
	v_pk_mul_f32 v[14:15], v[18:19], v[18:19]
	v_lshlrev_b32_e32 v16, 16, v12
	v_add_f32_dpp v31, v31, v31 quad_perm:[2,3,0,1] row_mask:0xf bank_mask:0xf bound_ctrl:1
	v_add_f32_e32 v49, v14, v15
	v_and_b32_e32 v17, 0xffff0000, v12
	v_add_f32_dpp v31, v31, v31 row_half_mirror row_mask:0xf bank_mask:0xf bound_ctrl:1
	v_pk_mul_f32 v[12:13], v[16:17], v[16:17]
	v_lshlrev_b32_e32 v14, 16, v11
	v_add_f32_dpp v31, v31, v31 row_mirror row_mask:0xf bank_mask:0xf bound_ctrl:1
	v_add_f32_e32 v50, v12, v13
	v_readlane_b32 s25, v31, 0
	v_readlane_b32 s50, v31, 16
	v_readlane_b32 s27, v31, 32
	v_readlane_b32 s46, v31, 48
	v_add_f32_dpp v31, v48, v48 quad_perm:[1,0,3,2] row_mask:0xf bank_mask:0xf bound_ctrl:1
	v_and_b32_e32 v15, 0xffff0000, v11
	v_pk_mul_f32 v[12:13], v[14:15], v[14:15]
	v_add_f32_dpp v31, v31, v31 quad_perm:[2,3,0,1] row_mask:0xf bank_mask:0xf bound_ctrl:1
	v_add_f32_e32 v51, v12, v13
	v_lshlrev_b32_e32 v12, 16, v10
	v_add_f32_dpp v31, v31, v31 row_half_mirror row_mask:0xf bank_mask:0xf bound_ctrl:1
	v_and_b32_e32 v13, 0xffff0000, v10
	v_pk_mul_f32 v[10:11], v[12:13], v[12:13]
	v_add_f32_dpp v31, v31, v31 row_mirror row_mask:0xf bank_mask:0xf bound_ctrl:1
	v_add_f32_e32 v52, v10, v11
	v_readlane_b32 s24, v31, 0
	v_readlane_b32 s61, v31, 16
	v_readlane_b32 s26, v31, 32
	v_readlane_b32 s58, v31, 48
	v_add_f32_dpp v31, v49, v49 quad_perm:[1,0,3,2] row_mask:0xf bank_mask:0xf bound_ctrl:1
	v_lshlrev_b32_e32 v10, 16, v8
	v_and_b32_e32 v11, 0xffff0000, v8
	v_add_f32_dpp v31, v31, v31 quad_perm:[2,3,0,1] row_mask:0xf bank_mask:0xf bound_ctrl:1
	v_pk_mul_f32 v[32:33], v[10:11], v[10:11]
	v_lshlrev_b32_e32 v8, 16, v9
	v_add_f32_dpp v31, v31, v31 row_half_mirror row_mask:0xf bank_mask:0xf bound_ctrl:1
	v_add_f32_e32 v53, v32, v33
	v_and_b32_e32 v9, 0xffff0000, v9
	v_add_f32_dpp v31, v31, v31 row_mirror row_mask:0xf bank_mask:0xf bound_ctrl:1
	v_pk_mul_f32 v[32:33], v[8:9], v[8:9]
	v_readlane_b32 s29, v31, 0
	v_readlane_b32 s51, v31, 16
	v_readlane_b32 s31, v31, 32
	v_readlane_b32 s47, v31, 48
	v_add_f32_dpp v31, v50, v50 quad_perm:[1,0,3,2] row_mask:0xf bank_mask:0xf bound_ctrl:1
	v_add_f32_e32 v32, v32, v33
	v_and_b32_e32 v33, 0xffff0000, v30
	v_add_f32_dpp v31, v31, v31 quad_perm:[2,3,0,1] row_mask:0xf bank_mask:0xf bound_ctrl:1
	s_nop 1
	v_add_f32_dpp v31, v31, v31 row_half_mirror row_mask:0xf bank_mask:0xf bound_ctrl:1
	s_nop 1
	v_add_f32_dpp v31, v31, v31 row_mirror row_mask:0xf bank_mask:0xf bound_ctrl:1
	s_nop 0
	v_readlane_b32 s28, v31, 0
	v_readlane_b32 s62, v31, 16
	v_readlane_b32 s30, v31, 32
	v_readlane_b32 s59, v31, 48
	v_add_f32_dpp v31, v51, v51 quad_perm:[1,0,3,2] row_mask:0xf bank_mask:0xf bound_ctrl:1
	s_nop 1
	v_add_f32_dpp v31, v31, v31 quad_perm:[2,3,0,1] row_mask:0xf bank_mask:0xf bound_ctrl:1
	s_nop 1
	v_add_f32_dpp v31, v31, v31 row_half_mirror row_mask:0xf bank_mask:0xf bound_ctrl:1
	s_nop 1
	v_add_f32_dpp v31, v31, v31 row_mirror row_mask:0xf bank_mask:0xf bound_ctrl:1
	s_nop 0
	v_readlane_b32 s35, v31, 0
	v_readlane_b32 s56, v31, 16
	v_readlane_b32 s37, v31, 32
	v_readlane_b32 s48, v31, 48
	v_add_f32_dpp v31, v52, v52 quad_perm:[1,0,3,2] row_mask:0xf bank_mask:0xf bound_ctrl:1
	s_nop 1
	v_add_f32_dpp v31, v31, v31 quad_perm:[2,3,0,1] row_mask:0xf bank_mask:0xf bound_ctrl:1
	s_nop 1
	v_add_f32_dpp v31, v31, v31 row_half_mirror row_mask:0xf bank_mask:0xf bound_ctrl:1
	s_nop 1
	v_add_f32_dpp v31, v31, v31 row_mirror row_mask:0xf bank_mask:0xf bound_ctrl:1
	s_nop 0
	v_readlane_b32 s34, v31, 0
	v_readlane_b32 s63, v31, 16
	v_readlane_b32 s36, v31, 32
	v_readlane_b32 s60, v31, 48
	v_add_f32_dpp v31, v53, v53 quad_perm:[1,0,3,2] row_mask:0xf bank_mask:0xf bound_ctrl:1
	s_nop 1
	v_add_f32_dpp v31, v31, v31 quad_perm:[2,3,0,1] row_mask:0xf bank_mask:0xf bound_ctrl:1
	s_nop 1
	v_add_f32_dpp v31, v31, v31 row_half_mirror row_mask:0xf bank_mask:0xf bound_ctrl:1
	s_nop 1
	v_add_f32_dpp v31, v31, v31 row_mirror row_mask:0xf bank_mask:0xf bound_ctrl:1
	s_nop 0
	v_readlane_b32 s39, v31, 0
	v_readlane_b32 s57, v31, 16
	v_readlane_b32 s41, v31, 32
	v_readlane_b32 s49, v31, 48
	v_add_f32_dpp v31, v32, v32 quad_perm:[1,0,3,2] row_mask:0xf bank_mask:0xf bound_ctrl:1
	v_lshlrev_b32_e32 v32, 16, v30
	s_nop 0
	v_add_f32_dpp v31, v31, v31 quad_perm:[2,3,0,1] row_mask:0xf bank_mask:0xf bound_ctrl:1
	s_nop 1
	v_add_f32_dpp v31, v31, v31 row_half_mirror row_mask:0xf bank_mask:0xf bound_ctrl:1
	s_nop 1
	v_add_f32_dpp v47, v31, v31 row_mirror row_mask:0xf bank_mask:0xf bound_ctrl:1
	v_pk_mul_f32 v[30:31], v[32:33], v[32:33]
	v_readlane_b32 s38, v47, 0
	v_add_f32_e32 v30, v30, v31
	v_readlane_b32 s65, v47, 16
	v_readlane_b32 s40, v47, 32
	v_add_f32_dpp v30, v30, v30 quad_perm:[1,0,3,2] row_mask:0xf bank_mask:0xf bound_ctrl:1
	v_readlane_b32 s64, v47, 48
	v_mbcnt_hi_u32_b32 v47, -1, v36
	v_add_f32_dpp v30, v30, v30 quad_perm:[2,3,0,1] row_mask:0xf bank_mask:0xf bound_ctrl:1
	s_nop 1
	v_add_f32_dpp v30, v30, v30 row_half_mirror row_mask:0xf bank_mask:0xf bound_ctrl:1
	s_nop 1
	v_add_f32_dpp v30, v30, v30 row_mirror row_mask:0xf bank_mask:0xf bound_ctrl:1
	s_nop 0
	v_readlane_b32 s0, v30, 16
	v_readlane_b32 s1, v30, 48
	v_readlane_b32 s8, v30, 0
	v_readlane_b32 s9, v30, 32
	v_mov_b32_e32 v30, s0
	v_mov_b32_e32 v31, s1
	v_pk_add_f32 v[30:31], s[8:9], v[30:31]
	s_nop 0
	v_add_f32_e32 v30, v30, v31
	v_fmamk_f32 v30, v30, 0x3c000000, v35
	v_mul_f32_e32 v31, 0x4b800000, v30
	v_cmp_gt_f32_e32 vcc, s44, v30
	s_nop 1
	v_cndmask_b32_e32 v30, v30, v31, vcc
	v_rsq_f32_e32 v30, v30
	s_nop 0
	v_mul_f32_e32 v31, 0x45800000, v30
	v_cndmask_b32_e32 v30, v30, v31, vcc
	v_pk_mul_f32 v[30:31], v[30:31], v[32:33] op_sel_hi:[0,1]
	v_cndmask_b32_e64 v32, 0, 1, s[10:11]
	v_pk_mul_f32 v[30:31], v[6:7], v[30:31]
	v_cmp_ne_u32_e64 s[8:9], 1, v32
	s_andn2_b64 vcc, exec, s[10:11]
	s_cbranch_vccnz .LBB0_506
	v_and_b32_e32 v33, 64, v47
	v_xor_b32_e32 v32, 16, v47
	v_add_u32_e32 v33, 64, v33
	v_cmp_lt_i32_e32 vcc, v32, v33
	s_nop 1
	v_cndmask_b32_e32 v32, v47, v32, vcc
	v_lshlrev_b32_e32 v33, 2, v32
	ds_bpermute_b32 v32, v33, v30
	ds_bpermute_b32 v33, v33, v31
	s_waitcnt lgkmcnt(0)
	v_pk_mul_f32 v[32:33], v[26:27], v[32:33]
	s_nop 0
	v_cndmask_b32_e64 v33, v33, -v33, s[6:7]
	v_cndmask_b32_e64 v32, v32, -v32, s[6:7]
	v_pk_fma_f32 v[30:31], v[24:25], v[30:31], v[32:33]
